# adds packed-f32 MoE up epilogue and the mixer queue-head check (skip fetch-and-add on exhausted queues) to the counted-lgkmcnt K loops
# speedup vs baseline: 1.0150x; 1.0040x over previous
.LBB0_1419:
	ds_read_b128 v[10:13], v130
	ds_read_b128 v[14:17], v130 offset:1024
	ds_read_b128 v[160:163], v130 offset:2048
	ds_read_b128 v[164:167], v130 offset:3072
	s_add_u32 s60, s18, 0xfffe0080
	s_addc_u32 s61, s19, -1
	s_cmp_eq_u32 s75, 4
	s_cselect_b32 s63, s15, s61
	s_cselect_b32 s62, s14, s60
	s_cselect_b32 s61, s17, s74
	s_cselect_b32 s60, s16, s73
	s_mov_b32 m0, s13
	v_lshl_add_u64 v[2:3], s[18:19], 0, v[156:157]
	ds_read_b128 v[178:181], v170
	ds_read_b128 v[182:185], v170 offset:1024
	ds_read_b128 v[186:189], v170 offset:2048
	ds_read_b128 v[190:193], v170 offset:3072
	ds_read_b128 v[194:197], v170 offset:4096
	ds_read_b128 v[198:201], v170 offset:5120
	ds_read_b128 v[218:221], v170 offset:6144
	ds_read_b128 v[222:225], v170 offset:7168
	global_load_lds_dwordx4 v[2:3], off
	v_lshl_add_u64 v[2:3], s[18:19], 0, v[158:159]
	s_mov_b32 m0, s64
	s_nop 0
	global_load_lds_dwordx4 v[2:3], off
	s_waitcnt lgkmcnt(8)
	s_waitcnt vmcnt(10)
	s_barrier
	s_setprio 1
	s_waitcnt lgkmcnt(6)
	v_mfma_scale_f32_16x16x128_f8f6f4 v[140:143], v[10:17], v[178:185], v[140:143], v205, v205 op_sel_hi:[0,0,0]
	v_mfma_scale_f32_16x16x128_f8f6f4 v[132:135], v[160:167], v[178:185], v[132:135], v205, v205 op_sel_hi:[0,0,0]
	s_waitcnt lgkmcnt(4)
	v_mfma_scale_f32_16x16x128_f8f6f4 v[122:125], v[10:17], v[186:193], v[122:125], v205, v205 op_sel_hi:[0,0,0]
	v_mfma_scale_f32_16x16x128_f8f6f4 v[114:117], v[160:167], v[186:193], v[114:117], v205, v205 op_sel_hi:[0,0,0]
	s_waitcnt lgkmcnt(2)
	v_mfma_scale_f32_16x16x128_f8f6f4 v[106:109], v[10:17], v[194:201], v[106:109], v205, v205 op_sel_hi:[0,0,0]
	v_mfma_scale_f32_16x16x128_f8f6f4 v[98:101], v[160:167], v[194:201], v[98:101], v205, v205 op_sel_hi:[0,0,0]
	s_waitcnt lgkmcnt(0)
	v_mfma_scale_f32_16x16x128_f8f6f4 v[90:93], v[10:17], v[218:225], v[90:93], v205, v205 op_sel_hi:[0,0,0]
	v_mfma_scale_f32_16x16x128_f8f6f4 v[78:81], v[160:167], v[218:225], v[78:81], v205, v205 op_sel_hi:[0,0,0]
	s_setprio 0
	s_barrier
	s_mov_b32 m0, s65
	v_lshl_add_u64 v[6:7], s[60:61], 0, v[154:155]
	ds_read_b128 v[226:229], v171
	ds_read_b128 v[230:233], v171 offset:1024
	ds_read_b128 v[234:237], v171 offset:2048
	ds_read_b128 v[238:241], v171 offset:3072
	global_load_lds_dwordx4 v[6:7], off
	v_lshl_add_u64 v[8:9], s[60:61], 0, v[150:151]
	s_mov_b32 m0, s66
	s_nop 0
	global_load_lds_dwordx4 v[8:9], off
	s_waitcnt vmcnt(10)
	s_barrier
	s_setprio 1
	s_waitcnt lgkmcnt(2)
	v_mfma_scale_f32_16x16x128_f8f6f4 v[144:147], v[226:233], v[178:185], v[144:147], v205, v205 op_sel_hi:[0,0,0]
	s_waitcnt lgkmcnt(0)
	v_mfma_scale_f32_16x16x128_f8f6f4 v[136:139], v[234:241], v[178:185], v[136:139], v205, v205 op_sel_hi:[0,0,0]
	v_mfma_scale_f32_16x16x128_f8f6f4 v[126:129], v[226:233], v[186:193], v[126:129], v205, v205 op_sel_hi:[0,0,0]
	v_mfma_scale_f32_16x16x128_f8f6f4 v[118:121], v[234:241], v[186:193], v[118:121], v205, v205 op_sel_hi:[0,0,0]
	v_mfma_scale_f32_16x16x128_f8f6f4 v[110:113], v[226:233], v[194:201], v[110:113], v205, v205 op_sel_hi:[0,0,0]
	v_mfma_scale_f32_16x16x128_f8f6f4 v[102:105], v[234:241], v[194:201], v[102:105], v205, v205 op_sel_hi:[0,0,0]
	v_mfma_scale_f32_16x16x128_f8f6f4 v[94:97], v[226:233], v[218:225], v[94:97], v205, v205 op_sel_hi:[0,0,0]
	v_mfma_scale_f32_16x16x128_f8f6f4 v[86:89], v[234:241], v[218:225], v[86:89], v205, v205 op_sel_hi:[0,0,0]
	s_setprio 0
	s_mov_b32 m0, s43
	v_lshl_add_u64 v[2:3], s[62:63], 0, v[152:153]
	s_barrier
	ds_read_b128 v[178:181], v170 offset:16384
	ds_read_b128 v[182:185], v170 offset:17408
	ds_read_b128 v[186:189], v170 offset:18432
	ds_read_b128 v[190:193], v170 offset:19456
	ds_read_b128 v[194:197], v170 offset:20480
	ds_read_b128 v[198:201], v170 offset:21504
	ds_read_b128 v[218:221], v170 offset:22528
	ds_read_b128 v[222:225], v170 offset:23552
	global_load_lds_dwordx4 v[2:3], off
	v_lshl_add_u64 v[4:5], s[62:63], 0, v[148:149]
	s_mov_b32 m0, s44
	s_nop 0
	global_load_lds_dwordx4 v[4:5], off
	s_barrier
	s_setprio 1
	s_waitcnt lgkmcnt(6)
	v_mfma_scale_f32_16x16x128_f8f6f4 v[74:77], v[10:17], v[178:185], v[74:77], v205, v205 op_sel_hi:[0,0,0]
	v_mfma_scale_f32_16x16x128_f8f6f4 v[66:69], v[160:167], v[178:185], v[66:69], v205, v205 op_sel_hi:[0,0,0]
	s_waitcnt lgkmcnt(4)
	v_mfma_scale_f32_16x16x128_f8f6f4 v[58:61], v[10:17], v[186:193], v[58:61], v205, v205 op_sel_hi:[0,0,0]
	v_mfma_scale_f32_16x16x128_f8f6f4 v[50:53], v[160:167], v[186:193], v[50:53], v205, v205 op_sel_hi:[0,0,0]
	s_waitcnt lgkmcnt(2)
	v_mfma_scale_f32_16x16x128_f8f6f4 v[42:45], v[10:17], v[194:201], v[42:45], v205, v205 op_sel_hi:[0,0,0]
	v_mfma_scale_f32_16x16x128_f8f6f4 v[34:37], v[160:167], v[194:201], v[34:37], v205, v205 op_sel_hi:[0,0,0]
	s_waitcnt lgkmcnt(0)
	v_mfma_scale_f32_16x16x128_f8f6f4 v[26:29], v[10:17], v[218:225], v[26:29], v205, v205 op_sel_hi:[0,0,0]
	v_mfma_scale_f32_16x16x128_f8f6f4 v[18:21], v[160:167], v[218:225], v[18:21], v205, v205 op_sel_hi:[0,0,0]
	s_setprio 0
	s_barrier
	s_add_u32 s76, s60, 0x2000
	s_addc_u32 s77, s61, 0
	s_mov_b32 m0, s67
	v_lshl_add_u64 v[10:11], s[76:77], 0, v[154:155]
	global_load_lds_dwordx4 v[10:11], off
	v_lshl_add_u64 v[10:11], s[76:77], 0, v[150:151]
	s_mov_b32 m0, s68
	s_nop 0
	global_load_lds_dwordx4 v[10:11], off
	s_waitcnt vmcnt(10)
	s_barrier
	s_setprio 1
	v_mfma_scale_f32_16x16x128_f8f6f4 v[82:85], v[226:233], v[178:185], v[82:85], v205, v205 op_sel_hi:[0,0,0]
	v_mfma_scale_f32_16x16x128_f8f6f4 v[70:73], v[234:241], v[178:185], v[70:73], v205, v205 op_sel_hi:[0,0,0]
	v_mfma_scale_f32_16x16x128_f8f6f4 v[62:65], v[226:233], v[186:193], v[62:65], v205, v205 op_sel_hi:[0,0,0]
	v_mfma_scale_f32_16x16x128_f8f6f4 v[54:57], v[234:241], v[186:193], v[54:57], v205, v205 op_sel_hi:[0,0,0]
	v_mfma_scale_f32_16x16x128_f8f6f4 v[46:49], v[226:233], v[194:201], v[46:49], v205, v205 op_sel_hi:[0,0,0]
	v_mfma_scale_f32_16x16x128_f8f6f4 v[38:41], v[234:241], v[194:201], v[38:41], v205, v205 op_sel_hi:[0,0,0]
	v_mfma_scale_f32_16x16x128_f8f6f4 v[30:33], v[226:233], v[218:225], v[30:33], v205, v205 op_sel_hi:[0,0,0]
	v_mfma_scale_f32_16x16x128_f8f6f4 v[22:25], v[234:241], v[218:225], v[22:25], v205, v205 op_sel_hi:[0,0,0]
	s_setprio 0
	s_barrier
	ds_read_b128 v[10:13], v172
	ds_read_b128 v[14:17], v172 offset:1024
	ds_read_b128 v[160:163], v172 offset:2048
	ds_read_b128 v[164:167], v172 offset:3072
	s_add_u32 s62, s62, 0x20000
	s_addc_u32 s63, s63, 0
	s_mov_b32 m0, s45
	v_lshl_add_u64 v[174:175], s[62:63], 0, v[152:153]
	ds_read_b128 v[178:181], v170 offset:32768
	ds_read_b128 v[182:185], v170 offset:33792
	ds_read_b128 v[186:189], v170 offset:34816
	ds_read_b128 v[190:193], v170 offset:35840
	ds_read_b128 v[194:197], v170 offset:36864
	ds_read_b128 v[198:201], v170 offset:37888
	ds_read_b128 v[218:221], v170 offset:38912
	ds_read_b128 v[222:225], v170 offset:39936
	global_load_lds_dwordx4 v[174:175], off
	v_lshl_add_u64 v[174:175], s[62:63], 0, v[148:149]
	s_mov_b32 m0, s46
	s_nop 0
	global_load_lds_dwordx4 v[174:175], off
	s_waitcnt lgkmcnt(8)
	s_waitcnt vmcnt(10)
	s_barrier
	s_setprio 1
	s_waitcnt lgkmcnt(6)
	v_mfma_scale_f32_16x16x128_f8f6f4 v[140:143], v[10:17], v[178:185], v[140:143], v205, v205 op_sel_hi:[0,0,0]
	v_mfma_scale_f32_16x16x128_f8f6f4 v[132:135], v[160:167], v[178:185], v[132:135], v205, v205 op_sel_hi:[0,0,0]
	s_waitcnt lgkmcnt(4)
	v_mfma_scale_f32_16x16x128_f8f6f4 v[122:125], v[10:17], v[186:193], v[122:125], v205, v205 op_sel_hi:[0,0,0]
	v_mfma_scale_f32_16x16x128_f8f6f4 v[114:117], v[160:167], v[186:193], v[114:117], v205, v205 op_sel_hi:[0,0,0]
	s_waitcnt lgkmcnt(2)
	v_mfma_scale_f32_16x16x128_f8f6f4 v[106:109], v[10:17], v[194:201], v[106:109], v205, v205 op_sel_hi:[0,0,0]
	v_mfma_scale_f32_16x16x128_f8f6f4 v[98:101], v[160:167], v[194:201], v[98:101], v205, v205 op_sel_hi:[0,0,0]
	s_waitcnt lgkmcnt(0)
	v_mfma_scale_f32_16x16x128_f8f6f4 v[90:93], v[10:17], v[218:225], v[90:93], v205, v205 op_sel_hi:[0,0,0]
	v_mfma_scale_f32_16x16x128_f8f6f4 v[78:81], v[160:167], v[218:225], v[78:81], v205, v205 op_sel_hi:[0,0,0]
	s_setprio 0
	s_barrier
	s_mov_b32 m0, s69
	v_lshl_add_u64 v[6:7], v[6:7], 0, s[30:31]
	ds_read_b128 v[226:229], v173
	ds_read_b128 v[230:233], v173 offset:1024
	ds_read_b128 v[234:237], v173 offset:2048
	ds_read_b128 v[238:241], v173 offset:3072
	global_load_lds_dwordx4 v[6:7], off
	v_lshl_add_u64 v[6:7], v[8:9], 0, s[30:31]
	s_mov_b32 m0, s70
	s_nop 0
	global_load_lds_dwordx4 v[6:7], off
	s_waitcnt vmcnt(10)
	s_barrier
	s_setprio 1
	s_waitcnt lgkmcnt(2)
	v_mfma_scale_f32_16x16x128_f8f6f4 v[144:147], v[226:233], v[178:185], v[144:147], v205, v205 op_sel_hi:[0,0,0]
	s_waitcnt lgkmcnt(0)
	v_mfma_scale_f32_16x16x128_f8f6f4 v[136:139], v[234:241], v[178:185], v[136:139], v205, v205 op_sel_hi:[0,0,0]
	v_mfma_scale_f32_16x16x128_f8f6f4 v[126:129], v[226:233], v[186:193], v[126:129], v205, v205 op_sel_hi:[0,0,0]
	v_mfma_scale_f32_16x16x128_f8f6f4 v[118:121], v[234:241], v[186:193], v[118:121], v205, v205 op_sel_hi:[0,0,0]
	v_mfma_scale_f32_16x16x128_f8f6f4 v[110:113], v[226:233], v[194:201], v[110:113], v205, v205 op_sel_hi:[0,0,0]
	v_mfma_scale_f32_16x16x128_f8f6f4 v[102:105], v[234:241], v[194:201], v[102:105], v205, v205 op_sel_hi:[0,0,0]
	v_mfma_scale_f32_16x16x128_f8f6f4 v[94:97], v[226:233], v[218:225], v[94:97], v205, v205 op_sel_hi:[0,0,0]
	v_mfma_scale_f32_16x16x128_f8f6f4 v[86:89], v[234:241], v[218:225], v[86:89], v205, v205 op_sel_hi:[0,0,0]
	s_setprio 0
	s_mov_b32 m0, s51
	v_lshl_add_u64 v[2:3], v[2:3], 0, s[30:31]
	s_barrier
	ds_read_b128 v[178:181], v170 offset:49152
	ds_read_b128 v[182:185], v170 offset:50176
	ds_read_b128 v[186:189], v170 offset:51200
	ds_read_b128 v[190:193], v170 offset:52224
	ds_read_b128 v[194:197], v170 offset:53248
	ds_read_b128 v[198:201], v170 offset:54272
	ds_read_b128 v[218:221], v170 offset:55296
	ds_read_b128 v[222:225], v170 offset:56320
	global_load_lds_dwordx4 v[2:3], off
	v_lshl_add_u64 v[2:3], v[4:5], 0, s[30:31]
	s_mov_b32 m0, s53
	s_nop 0
	global_load_lds_dwordx4 v[2:3], off
	s_barrier
	s_setprio 1
	s_waitcnt lgkmcnt(6)
	v_mfma_scale_f32_16x16x128_f8f6f4 v[74:77], v[10:17], v[178:185], v[74:77], v205, v205 op_sel_hi:[0,0,0]
	v_mfma_scale_f32_16x16x128_f8f6f4 v[66:69], v[160:167], v[178:185], v[66:69], v205, v205 op_sel_hi:[0,0,0]
	s_waitcnt lgkmcnt(4)
	v_mfma_scale_f32_16x16x128_f8f6f4 v[58:61], v[10:17], v[186:193], v[58:61], v205, v205 op_sel_hi:[0,0,0]
	v_mfma_scale_f32_16x16x128_f8f6f4 v[50:53], v[160:167], v[186:193], v[50:53], v205, v205 op_sel_hi:[0,0,0]
	s_waitcnt lgkmcnt(2)
	v_mfma_scale_f32_16x16x128_f8f6f4 v[42:45], v[10:17], v[194:201], v[42:45], v205, v205 op_sel_hi:[0,0,0]
	v_mfma_scale_f32_16x16x128_f8f6f4 v[34:37], v[160:167], v[194:201], v[34:37], v205, v205 op_sel_hi:[0,0,0]
	s_waitcnt lgkmcnt(0)
	v_mfma_scale_f32_16x16x128_f8f6f4 v[26:29], v[10:17], v[218:225], v[26:29], v205, v205 op_sel_hi:[0,0,0]
	v_mfma_scale_f32_16x16x128_f8f6f4 v[18:21], v[160:167], v[218:225], v[18:21], v205, v205 op_sel_hi:[0,0,0]
	s_setprio 0
	s_barrier
	s_add_u32 s60, s60, 0x2080
	s_addc_u32 s61, s61, 0
	s_mov_b32 m0, s71
	v_lshl_add_u64 v[2:3], s[60:61], 0, v[154:155]
	global_load_lds_dwordx4 v[2:3], off
	v_lshl_add_u64 v[2:3], s[60:61], 0, v[150:151]
	s_mov_b32 m0, s72
	s_nop 0
	global_load_lds_dwordx4 v[2:3], off
	s_waitcnt vmcnt(10)
	s_barrier
	s_setprio 1
	v_mfma_scale_f32_16x16x128_f8f6f4 v[82:85], v[226:233], v[178:185], v[82:85], v205, v205 op_sel_hi:[0,0,0]
	v_mfma_scale_f32_16x16x128_f8f6f4 v[70:73], v[234:241], v[178:185], v[70:73], v205, v205 op_sel_hi:[0,0,0]
	v_mfma_scale_f32_16x16x128_f8f6f4 v[62:65], v[226:233], v[186:193], v[62:65], v205, v205 op_sel_hi:[0,0,0]
	v_mfma_scale_f32_16x16x128_f8f6f4 v[54:57], v[234:241], v[186:193], v[54:57], v205, v205 op_sel_hi:[0,0,0]
	v_mfma_scale_f32_16x16x128_f8f6f4 v[46:49], v[226:233], v[194:201], v[46:49], v205, v205 op_sel_hi:[0,0,0]
	v_mfma_scale_f32_16x16x128_f8f6f4 v[38:41], v[234:241], v[194:201], v[38:41], v205, v205 op_sel_hi:[0,0,0]
	v_mfma_scale_f32_16x16x128_f8f6f4 v[30:33], v[226:233], v[218:225], v[30:33], v205, v205 op_sel_hi:[0,0,0]
	v_mfma_scale_f32_16x16x128_f8f6f4 v[22:25], v[234:241], v[218:225], v[22:25], v205, v205 op_sel_hi:[0,0,0]
	s_setprio 0
	s_add_i32 s75, s75, 2
	s_add_u32 s18, s18, 0x100
	s_addc_u32 s19, s19, 0
	s_add_u32 s73, s73, 0x100
	s_addc_u32 s74, s74, 0
	s_cmp_gt_u32 s75, 5
	s_barrier
	s_cbranch_scc0 .LBB0_1419
	v_mov_b32_e32 v234, 0xbcb8aa3b
	v_mov_b32_e32 v235, 0xbcb8aa3b
	v_mov_b32_e32 v236, 1.0
	v_mov_b32_e32 v237, 1.0
	v_mov_b32_e32 v238, 0x3b000000
	v_mov_b32_e32 v239, 0x3b000000
	v_pk_mul_f32 v[218:219], v[140:141], v[234:235]
	v_pk_mul_f32 v[220:221], v[142:143], v[234:235]
	v_pk_mul_f32 v[226:227], v[132:133], v[234:235]
	v_pk_mul_f32 v[228:229], v[134:135], v[234:235]
	v_exp_f32_e32 v218, v218
	v_exp_f32_e32 v219, v219
	v_exp_f32_e32 v220, v220
	v_exp_f32_e32 v221, v221
	v_exp_f32_e32 v226, v226
	v_exp_f32_e32 v227, v227
	v_exp_f32_e32 v228, v228
	v_exp_f32_e32 v229, v229
	v_pk_mul_f32 v[222:223], v[140:141], v[144:145]
	v_pk_mul_f32 v[224:225], v[142:143], v[146:147]
	v_pk_mul_f32 v[230:231], v[132:133], v[136:137]
	v_pk_mul_f32 v[232:233], v[134:135], v[138:139]
	v_pk_add_f32 v[218:219], v[236:237], v[218:219]
	v_pk_add_f32 v[220:221], v[236:237], v[220:221]
	v_pk_add_f32 v[226:227], v[236:237], v[226:227]
	v_pk_add_f32 v[228:229], v[236:237], v[228:229]
	v_rcp_f32_e32 v218, v218
	v_rcp_f32_e32 v219, v219
	v_rcp_f32_e32 v220, v220
	v_rcp_f32_e32 v221, v221
	v_rcp_f32_e32 v226, v226
	v_rcp_f32_e32 v227, v227
	v_rcp_f32_e32 v228, v228
	v_rcp_f32_e32 v229, v229
	v_pk_mul_f32 v[222:223], v[238:239], v[222:223]
	v_pk_mul_f32 v[224:225], v[238:239], v[224:225]
	v_pk_mul_f32 v[230:231], v[238:239], v[230:231]
	v_pk_mul_f32 v[232:233], v[238:239], v[232:233]
	v_pk_mul_f32 v[222:223], v[218:219], v[222:223]
	v_pk_mul_f32 v[224:225], v[220:221], v[224:225]
	v_pk_mul_f32 v[230:231], v[226:227], v[230:231]
	v_pk_mul_f32 v[232:233], v[228:229], v[232:233]
	v_med3_f32 v222, v222, s26, v209
	v_med3_f32 v223, v223, s26, v209
	v_med3_f32 v224, v224, s26, v209
	v_med3_f32 v225, v225, s26, v209
	v_med3_f32 v230, v230, s26, v209
	v_med3_f32 v231, v231, s26, v209
	v_med3_f32 v232, v232, s26, v209
	v_med3_f32 v233, v233, s26, v209
	v_cvt_pk_fp8_f32 v4, v222, v223
	v_cvt_pk_fp8_f32 v4, v224, v225 op_sel:[0,0,1]
	v_cvt_pk_fp8_f32 v5, v230, v231
	v_cvt_pk_fp8_f32 v5, v232, v233 op_sel:[0,0,1]
	s_ashr_i32 s13, s12, 31
	s_lshl_b64 s[12:13], s[12:13], 11
	s_add_u32 s12, s47, s12
	s_addc_u32 s13, s50, s13
	s_ashr_i32 s14, s59, 31
	s_add_u32 s12, s12, s59
	s_addc_u32 s13, s13, s14
	v_mov_b32_e32 v130, v169
	s_nop 15
	s_nop 15
	global_store_dwordx2 v130, v[4:5], s[12:13]
	v_pk_mul_f32 v[218:219], v[122:123], v[234:235]
	v_pk_mul_f32 v[220:221], v[124:125], v[234:235]
	v_pk_mul_f32 v[226:227], v[114:115], v[234:235]
	v_pk_mul_f32 v[228:229], v[116:117], v[234:235]
	v_exp_f32_e32 v218, v218
	v_exp_f32_e32 v219, v219
	v_exp_f32_e32 v220, v220
	v_exp_f32_e32 v221, v221
	v_exp_f32_e32 v226, v226
	v_exp_f32_e32 v227, v227
	v_exp_f32_e32 v228, v228
	v_exp_f32_e32 v229, v229
	v_pk_mul_f32 v[222:223], v[122:123], v[126:127]
	v_pk_mul_f32 v[224:225], v[124:125], v[128:129]
	v_pk_mul_f32 v[230:231], v[114:115], v[118:119]
	v_pk_mul_f32 v[232:233], v[116:117], v[120:121]
	v_pk_add_f32 v[218:219], v[236:237], v[218:219]
	v_pk_add_f32 v[220:221], v[236:237], v[220:221]
	v_pk_add_f32 v[226:227], v[236:237], v[226:227]
	v_pk_add_f32 v[228:229], v[236:237], v[228:229]
	v_rcp_f32_e32 v218, v218
	v_rcp_f32_e32 v219, v219
	v_rcp_f32_e32 v220, v220
	v_rcp_f32_e32 v221, v221
	v_rcp_f32_e32 v226, v226
	v_rcp_f32_e32 v227, v227
	v_rcp_f32_e32 v228, v228
	v_rcp_f32_e32 v229, v229
	v_pk_mul_f32 v[222:223], v[238:239], v[222:223]
	v_pk_mul_f32 v[224:225], v[238:239], v[224:225]
	v_pk_mul_f32 v[230:231], v[238:239], v[230:231]
	v_pk_mul_f32 v[232:233], v[238:239], v[232:233]
	v_pk_mul_f32 v[222:223], v[218:219], v[222:223]
	v_pk_mul_f32 v[224:225], v[220:221], v[224:225]
	v_pk_mul_f32 v[230:231], v[226:227], v[230:231]
	v_pk_mul_f32 v[232:233], v[228:229], v[232:233]
	v_med3_f32 v222, v222, s26, v209
	v_med3_f32 v223, v223, s26, v209
	v_med3_f32 v224, v224, s26, v209
	v_med3_f32 v225, v225, s26, v209
	v_med3_f32 v230, v230, s26, v209
	v_med3_f32 v231, v231, s26, v209
	v_med3_f32 v232, v232, s26, v209
	v_med3_f32 v233, v233, s26, v209
	v_cvt_pk_fp8_f32 v4, v222, v223
	v_cvt_pk_fp8_f32 v4, v224, v225 op_sel:[0,0,1]
	v_cvt_pk_fp8_f32 v5, v230, v231
	v_cvt_pk_fp8_f32 v5, v232, v233 op_sel:[0,0,1]
	v_lshl_add_u64 v[2:3], s[12:13], 0, v[130:131]
	s_mov_b32 s12, 0x8000
	v_add_co_u32_e32 v6, vcc, s12, v2
	s_nop 0
	v_addc_co_u32_e32 v7, vcc, 0, v3, vcc
	global_store_dwordx2 v[6:7], v[4:5], off
	v_pk_mul_f32 v[218:219], v[106:107], v[234:235]
	v_pk_mul_f32 v[220:221], v[108:109], v[234:235]
	v_pk_mul_f32 v[226:227], v[98:99], v[234:235]
	v_pk_mul_f32 v[228:229], v[100:101], v[234:235]
	v_exp_f32_e32 v218, v218
	v_exp_f32_e32 v219, v219
	v_exp_f32_e32 v220, v220
	v_exp_f32_e32 v221, v221
	v_exp_f32_e32 v226, v226
	v_exp_f32_e32 v227, v227
	v_exp_f32_e32 v228, v228
	v_exp_f32_e32 v229, v229
	v_pk_mul_f32 v[222:223], v[106:107], v[110:111]
	v_pk_mul_f32 v[224:225], v[108:109], v[112:113]
	v_pk_mul_f32 v[230:231], v[98:99], v[102:103]
	v_pk_mul_f32 v[232:233], v[100:101], v[104:105]
	v_pk_add_f32 v[218:219], v[236:237], v[218:219]
	v_pk_add_f32 v[220:221], v[236:237], v[220:221]
	v_pk_add_f32 v[226:227], v[236:237], v[226:227]
	v_pk_add_f32 v[228:229], v[236:237], v[228:229]
	v_rcp_f32_e32 v218, v218
	v_rcp_f32_e32 v219, v219
	v_rcp_f32_e32 v220, v220
	v_rcp_f32_e32 v221, v221
	v_rcp_f32_e32 v226, v226
	v_rcp_f32_e32 v227, v227
	v_rcp_f32_e32 v228, v228
	v_rcp_f32_e32 v229, v229
	v_pk_mul_f32 v[222:223], v[238:239], v[222:223]
	v_pk_mul_f32 v[224:225], v[238:239], v[224:225]
	v_pk_mul_f32 v[230:231], v[238:239], v[230:231]
	v_pk_mul_f32 v[232:233], v[238:239], v[232:233]
	v_pk_mul_f32 v[222:223], v[218:219], v[222:223]
	v_pk_mul_f32 v[224:225], v[220:221], v[224:225]
	v_pk_mul_f32 v[230:231], v[226:227], v[230:231]
	v_pk_mul_f32 v[232:233], v[228:229], v[232:233]
	v_med3_f32 v222, v222, s26, v209
	v_med3_f32 v223, v223, s26, v209
	v_med3_f32 v224, v224, s26, v209
	v_med3_f32 v225, v225, s26, v209
	v_med3_f32 v230, v230, s26, v209
	v_med3_f32 v231, v231, s26, v209
	v_med3_f32 v232, v232, s26, v209
	v_med3_f32 v233, v233, s26, v209
	v_cvt_pk_fp8_f32 v4, v222, v223
	v_cvt_pk_fp8_f32 v4, v224, v225 op_sel:[0,0,1]
	v_cvt_pk_fp8_f32 v5, v230, v231
	v_cvt_pk_fp8_f32 v5, v232, v233 op_sel:[0,0,1]
	s_mov_b32 s12, 0x10000
	v_add_co_u32_e32 v6, vcc, s12, v2
	s_nop 0
	v_addc_co_u32_e32 v7, vcc, 0, v3, vcc
	global_store_dwordx2 v[6:7], v[4:5], off
	v_pk_mul_f32 v[218:219], v[90:91], v[234:235]
	v_pk_mul_f32 v[220:221], v[92:93], v[234:235]
	v_pk_mul_f32 v[226:227], v[78:79], v[234:235]
	v_pk_mul_f32 v[228:229], v[80:81], v[234:235]
	v_exp_f32_e32 v218, v218
	v_exp_f32_e32 v219, v219
	v_exp_f32_e32 v220, v220
	v_exp_f32_e32 v221, v221
	v_exp_f32_e32 v226, v226
	v_exp_f32_e32 v227, v227
	v_exp_f32_e32 v228, v228
	v_exp_f32_e32 v229, v229
	v_pk_mul_f32 v[222:223], v[90:91], v[94:95]
	v_pk_mul_f32 v[224:225], v[92:93], v[96:97]
	v_pk_mul_f32 v[230:231], v[78:79], v[86:87]
	v_pk_mul_f32 v[232:233], v[80:81], v[88:89]
	v_pk_add_f32 v[218:219], v[236:237], v[218:219]
	v_pk_add_f32 v[220:221], v[236:237], v[220:221]
	v_pk_add_f32 v[226:227], v[236:237], v[226:227]
	v_pk_add_f32 v[228:229], v[236:237], v[228:229]
	v_rcp_f32_e32 v218, v218
	v_rcp_f32_e32 v219, v219
	v_rcp_f32_e32 v220, v220
	v_rcp_f32_e32 v221, v221
	v_rcp_f32_e32 v226, v226
	v_rcp_f32_e32 v227, v227
	v_rcp_f32_e32 v228, v228
	v_rcp_f32_e32 v229, v229
	v_pk_mul_f32 v[222:223], v[238:239], v[222:223]
	v_pk_mul_f32 v[224:225], v[238:239], v[224:225]
	v_pk_mul_f32 v[230:231], v[238:239], v[230:231]
	v_pk_mul_f32 v[232:233], v[238:239], v[232:233]
	v_pk_mul_f32 v[222:223], v[218:219], v[222:223]
	v_pk_mul_f32 v[224:225], v[220:221], v[224:225]
	v_pk_mul_f32 v[230:231], v[226:227], v[230:231]
	v_pk_mul_f32 v[232:233], v[228:229], v[232:233]
	v_med3_f32 v222, v222, s26, v209
	v_med3_f32 v223, v223, s26, v209
	v_med3_f32 v224, v224, s26, v209
	v_med3_f32 v225, v225, s26, v209
	v_med3_f32 v230, v230, s26, v209
	v_med3_f32 v231, v231, s26, v209
	v_med3_f32 v232, v232, s26, v209
	v_med3_f32 v233, v233, s26, v209
	v_cvt_pk_fp8_f32 v4, v222, v223
	v_cvt_pk_fp8_f32 v4, v224, v225 op_sel:[0,0,1]
	v_cvt_pk_fp8_f32 v5, v230, v231
	v_cvt_pk_fp8_f32 v5, v232, v233 op_sel:[0,0,1]
	s_mov_b32 s12, 0x18000
	v_add_co_u32_e32 v6, vcc, s12, v2
	s_nop 0
	v_addc_co_u32_e32 v7, vcc, 0, v3, vcc
	global_store_dwordx2 v[6:7], v[4:5], off
	v_pk_mul_f32 v[218:219], v[74:75], v[234:235]
	v_pk_mul_f32 v[220:221], v[76:77], v[234:235]
	v_pk_mul_f32 v[226:227], v[66:67], v[234:235]
	v_pk_mul_f32 v[228:229], v[68:69], v[234:235]
	v_exp_f32_e32 v218, v218
	v_exp_f32_e32 v219, v219
	v_exp_f32_e32 v220, v220
	v_exp_f32_e32 v221, v221
	v_exp_f32_e32 v226, v226
	v_exp_f32_e32 v227, v227
	v_exp_f32_e32 v228, v228
	v_exp_f32_e32 v229, v229
	v_pk_mul_f32 v[222:223], v[74:75], v[82:83]
	v_pk_mul_f32 v[224:225], v[76:77], v[84:85]
	v_pk_mul_f32 v[230:231], v[66:67], v[70:71]
	v_pk_mul_f32 v[232:233], v[68:69], v[72:73]
	v_pk_add_f32 v[218:219], v[236:237], v[218:219]
	v_pk_add_f32 v[220:221], v[236:237], v[220:221]
	v_pk_add_f32 v[226:227], v[236:237], v[226:227]
	v_pk_add_f32 v[228:229], v[236:237], v[228:229]
	v_rcp_f32_e32 v218, v218
	v_rcp_f32_e32 v219, v219
	v_rcp_f32_e32 v220, v220
	v_rcp_f32_e32 v221, v221
	v_rcp_f32_e32 v226, v226
	v_rcp_f32_e32 v227, v227
	v_rcp_f32_e32 v228, v228
	v_rcp_f32_e32 v229, v229
	v_pk_mul_f32 v[222:223], v[238:239], v[222:223]
	v_pk_mul_f32 v[224:225], v[238:239], v[224:225]
	v_pk_mul_f32 v[230:231], v[238:239], v[230:231]
	v_pk_mul_f32 v[232:233], v[238:239], v[232:233]
	v_pk_mul_f32 v[222:223], v[218:219], v[222:223]
	v_pk_mul_f32 v[224:225], v[220:221], v[224:225]
	v_pk_mul_f32 v[230:231], v[226:227], v[230:231]
	v_pk_mul_f32 v[232:233], v[228:229], v[232:233]
	v_med3_f32 v222, v222, s26, v209
	v_med3_f32 v223, v223, s26, v209
	v_med3_f32 v224, v224, s26, v209
	v_med3_f32 v225, v225, s26, v209
	v_med3_f32 v230, v230, s26, v209
	v_med3_f32 v231, v231, s26, v209
	v_med3_f32 v232, v232, s26, v209
	v_med3_f32 v233, v233, s26, v209
	v_cvt_pk_fp8_f32 v4, v222, v223
	v_cvt_pk_fp8_f32 v4, v224, v225 op_sel:[0,0,1]
	v_cvt_pk_fp8_f32 v5, v230, v231
	v_cvt_pk_fp8_f32 v5, v232, v233 op_sel:[0,0,1]
	s_mov_b32 s12, 0x40000
	v_add_co_u32_e32 v6, vcc, s12, v2
	s_nop 0
	v_addc_co_u32_e32 v7, vcc, 0, v3, vcc
	global_store_dwordx2 v[6:7], v[4:5], off
	v_pk_mul_f32 v[218:219], v[58:59], v[234:235]
	v_pk_mul_f32 v[220:221], v[60:61], v[234:235]
	v_pk_mul_f32 v[226:227], v[50:51], v[234:235]
	v_pk_mul_f32 v[228:229], v[52:53], v[234:235]
	v_exp_f32_e32 v218, v218
	v_exp_f32_e32 v219, v219
	v_exp_f32_e32 v220, v220
	v_exp_f32_e32 v221, v221
	v_exp_f32_e32 v226, v226
	v_exp_f32_e32 v227, v227
	v_exp_f32_e32 v228, v228
	v_exp_f32_e32 v229, v229
	v_pk_mul_f32 v[222:223], v[58:59], v[62:63]
	v_pk_mul_f32 v[224:225], v[60:61], v[64:65]
	v_pk_mul_f32 v[230:231], v[50:51], v[54:55]
	v_pk_mul_f32 v[232:233], v[52:53], v[56:57]
	v_pk_add_f32 v[218:219], v[236:237], v[218:219]
	v_pk_add_f32 v[220:221], v[236:237], v[220:221]
	v_pk_add_f32 v[226:227], v[236:237], v[226:227]
	v_pk_add_f32 v[228:229], v[236:237], v[228:229]
	v_rcp_f32_e32 v218, v218
	v_rcp_f32_e32 v219, v219
	v_rcp_f32_e32 v220, v220
	v_rcp_f32_e32 v221, v221
	v_rcp_f32_e32 v226, v226
	v_rcp_f32_e32 v227, v227
	v_rcp_f32_e32 v228, v228
	v_rcp_f32_e32 v229, v229
	v_pk_mul_f32 v[222:223], v[238:239], v[222:223]
	v_pk_mul_f32 v[224:225], v[238:239], v[224:225]
	v_pk_mul_f32 v[230:231], v[238:239], v[230:231]
	v_pk_mul_f32 v[232:233], v[238:239], v[232:233]
	v_pk_mul_f32 v[222:223], v[218:219], v[222:223]
	v_pk_mul_f32 v[224:225], v[220:221], v[224:225]
	v_pk_mul_f32 v[230:231], v[226:227], v[230:231]
	v_pk_mul_f32 v[232:233], v[228:229], v[232:233]
	v_med3_f32 v222, v222, s26, v209
	v_med3_f32 v223, v223, s26, v209
	v_med3_f32 v224, v224, s26, v209
	v_med3_f32 v225, v225, s26, v209
	v_med3_f32 v230, v230, s26, v209
	v_med3_f32 v231, v231, s26, v209
	v_med3_f32 v232, v232, s26, v209
	v_med3_f32 v233, v233, s26, v209
	v_cvt_pk_fp8_f32 v4, v222, v223
	v_cvt_pk_fp8_f32 v4, v224, v225 op_sel:[0,0,1]
	v_cvt_pk_fp8_f32 v5, v230, v231
	v_cvt_pk_fp8_f32 v5, v232, v233 op_sel:[0,0,1]
	s_mov_b32 s12, 0x48000
	v_add_co_u32_e32 v6, vcc, s12, v2
	s_nop 0
	v_addc_co_u32_e32 v7, vcc, 0, v3, vcc
	global_store_dwordx2 v[6:7], v[4:5], off
	v_pk_mul_f32 v[218:219], v[42:43], v[234:235]
	v_pk_mul_f32 v[220:221], v[44:45], v[234:235]
	v_pk_mul_f32 v[226:227], v[34:35], v[234:235]
	v_pk_mul_f32 v[228:229], v[36:37], v[234:235]
	v_exp_f32_e32 v218, v218
	v_exp_f32_e32 v219, v219
	v_exp_f32_e32 v220, v220
	v_exp_f32_e32 v221, v221
	v_exp_f32_e32 v226, v226
	v_exp_f32_e32 v227, v227
	v_exp_f32_e32 v228, v228
	v_exp_f32_e32 v229, v229
	v_pk_mul_f32 v[222:223], v[42:43], v[46:47]
	v_pk_mul_f32 v[224:225], v[44:45], v[48:49]
	v_pk_mul_f32 v[230:231], v[34:35], v[38:39]
	v_pk_mul_f32 v[232:233], v[36:37], v[40:41]
	v_pk_add_f32 v[218:219], v[236:237], v[218:219]
	v_pk_add_f32 v[220:221], v[236:237], v[220:221]
	v_pk_add_f32 v[226:227], v[236:237], v[226:227]
	v_pk_add_f32 v[228:229], v[236:237], v[228:229]
	v_rcp_f32_e32 v218, v218
	v_rcp_f32_e32 v219, v219
	v_rcp_f32_e32 v220, v220
	v_rcp_f32_e32 v221, v221
	v_rcp_f32_e32 v226, v226
	v_rcp_f32_e32 v227, v227
	v_rcp_f32_e32 v228, v228
	v_rcp_f32_e32 v229, v229
	v_pk_mul_f32 v[222:223], v[238:239], v[222:223]
	v_pk_mul_f32 v[224:225], v[238:239], v[224:225]
	v_pk_mul_f32 v[230:231], v[238:239], v[230:231]
	v_pk_mul_f32 v[232:233], v[238:239], v[232:233]
	v_pk_mul_f32 v[222:223], v[218:219], v[222:223]
	v_pk_mul_f32 v[224:225], v[220:221], v[224:225]
	v_pk_mul_f32 v[230:231], v[226:227], v[230:231]
	v_pk_mul_f32 v[232:233], v[228:229], v[232:233]
	v_med3_f32 v222, v222, s26, v209
	v_med3_f32 v223, v223, s26, v209
	v_med3_f32 v224, v224, s26, v209
	v_med3_f32 v225, v225, s26, v209
	v_med3_f32 v230, v230, s26, v209
	v_med3_f32 v231, v231, s26, v209
	v_med3_f32 v232, v232, s26, v209
	v_med3_f32 v233, v233, s26, v209
	v_cvt_pk_fp8_f32 v4, v222, v223
	v_cvt_pk_fp8_f32 v4, v224, v225 op_sel:[0,0,1]
	v_cvt_pk_fp8_f32 v5, v230, v231
	v_cvt_pk_fp8_f32 v5, v232, v233 op_sel:[0,0,1]
	s_mov_b32 s12, 0x50000
	v_add_co_u32_e32 v6, vcc, s12, v2
	s_nop 0
	v_addc_co_u32_e32 v7, vcc, 0, v3, vcc
	global_store_dwordx2 v[6:7], v[4:5], off
	v_pk_mul_f32 v[218:219], v[26:27], v[234:235]
	v_pk_mul_f32 v[220:221], v[28:29], v[234:235]
	v_pk_mul_f32 v[226:227], v[18:19], v[234:235]
	v_pk_mul_f32 v[228:229], v[20:21], v[234:235]
	v_exp_f32_e32 v218, v218
	v_exp_f32_e32 v219, v219
	v_exp_f32_e32 v220, v220
	v_exp_f32_e32 v221, v221
	v_exp_f32_e32 v226, v226
	v_exp_f32_e32 v227, v227
	v_exp_f32_e32 v228, v228
	v_exp_f32_e32 v229, v229
	v_pk_mul_f32 v[222:223], v[26:27], v[30:31]
	v_pk_mul_f32 v[224:225], v[28:29], v[32:33]
	v_pk_mul_f32 v[230:231], v[18:19], v[22:23]
	v_pk_mul_f32 v[232:233], v[20:21], v[24:25]
	v_pk_add_f32 v[218:219], v[236:237], v[218:219]
	v_pk_add_f32 v[220:221], v[236:237], v[220:221]
	v_pk_add_f32 v[226:227], v[236:237], v[226:227]
	v_pk_add_f32 v[228:229], v[236:237], v[228:229]
	v_rcp_f32_e32 v218, v218
	v_rcp_f32_e32 v219, v219
	v_rcp_f32_e32 v220, v220
	v_rcp_f32_e32 v221, v221
	v_rcp_f32_e32 v226, v226
	v_rcp_f32_e32 v227, v227
	v_rcp_f32_e32 v228, v228
	v_rcp_f32_e32 v229, v229
	v_pk_mul_f32 v[222:223], v[238:239], v[222:223]
	v_pk_mul_f32 v[224:225], v[238:239], v[224:225]
	v_pk_mul_f32 v[230:231], v[238:239], v[230:231]
	v_pk_mul_f32 v[232:233], v[238:239], v[232:233]
	v_pk_mul_f32 v[222:223], v[218:219], v[222:223]
	v_pk_mul_f32 v[224:225], v[220:221], v[224:225]
	v_pk_mul_f32 v[230:231], v[226:227], v[230:231]
	v_pk_mul_f32 v[232:233], v[228:229], v[232:233]
	v_med3_f32 v222, v222, s26, v209
	v_med3_f32 v223, v223, s26, v209
	v_med3_f32 v224, v224, s26, v209
	v_med3_f32 v225, v225, s26, v209
	v_med3_f32 v230, v230, s26, v209
	v_med3_f32 v231, v231, s26, v209
	v_med3_f32 v232, v232, s26, v209
	v_med3_f32 v233, v233, s26, v209
	v_cvt_pk_fp8_f32 v4, v222, v223
	v_cvt_pk_fp8_f32 v4, v224, v225 op_sel:[0,0,1]
	v_cvt_pk_fp8_f32 v5, v230, v231
	v_cvt_pk_fp8_f32 v5, v232, v233 op_sel:[0,0,1]
	v_add_co_u32_e32 v2, vcc, 0x58000, v2
	s_nop 0
	v_addc_co_u32_e32 v3, vcc, 0, v3, vcc
	s_and_b64 vcc, exec, s[4:5]
	s_mov_b32 s12, s6
	s_mov_b32 s59, s7
	s_mov_b64 s[60:61], s[8:9]
	s_mov_b64 s[18:19], s[10:11]
	global_store_dwordx2 v[2:3], v[4:5], off
	s_cbranch_vccz .LBB0_1416
	s_waitcnt vmcnt(0)
	s_cmpk_gt_u32 s27, 0xff
	s_movk_i32 s47, 0x900
	s_cbranch_scc1 .LBB0_1423
	s_barrier
